# v34: scan step reads Q/att fragments in consumption order with per-MFMA-pair counted lgkmcnt waits
# speedup vs baseline: 1.0014x; 1.0014x over previous
.LBB0_571:
	s_andn2_b64 vcc, exec, s[0:1]
	s_cbranch_vccnz .LBB0_557
	ds_read_b128 v[66:69], v136
	ds_read_b128 v[70:73], v136 offset:8192
	ds_read_b128 v[114:117], v136 offset:1024
	ds_read_b128 v[150:153], v136 offset:9216
	ds_read_b128 v[118:121], v136 offset:2048
	ds_read_b128 v[154:157], v136 offset:10240
	ds_read_b128 v[122:125], v136 offset:3072
	ds_read_b128 v[158:161], v136 offset:11264
	ds_read_b128 v[126:129], v136 offset:4096
	ds_read_b128 v[162:165], v136 offset:12288
	ds_read_b128 v[138:141], v136 offset:5120
	ds_read_b128 v[166:169], v136 offset:13312
	ds_read_b128 v[142:145], v136 offset:6144
	ds_read_b128 v[170:173], v136 offset:14336
	ds_read_b128 v[146:149], v136 offset:7168
	ds_read_b128 v[174:177], v136 offset:15360
	ds_read_b128 v[178:181], v136 offset:32768
	ds_read_b128 v[198:201], v136 offset:36864
	ds_read_b128 v[182:185], v136 offset:33792
	ds_read_b128 v[202:205], v136 offset:37888
	ds_read_b128 v[186:189], v136 offset:34816
	ds_read_b128 v[206:209], v136 offset:38912
	ds_read_b128 v[190:193], v136 offset:35840
	ds_read_b128 v[210:213], v136 offset:39936
	v_cvt_pk_bf16_f32 v74, v2, v3
	v_cvt_pk_bf16_f32 v75, v4, v5
	v_cvt_pk_bf16_f32 v76, v6, v7
	v_cvt_pk_bf16_f32 v77, v8, v9
	v_cvt_pk_bf16_f32 v214, v10, v11
	v_cvt_pk_bf16_f32 v215, v12, v13
	v_cvt_pk_bf16_f32 v216, v14, v15
	v_cvt_pk_bf16_f32 v217, v16, v17
	v_cvt_pk_bf16_f32 v218, v18, v19
	v_cvt_pk_bf16_f32 v219, v20, v21
	v_cvt_pk_bf16_f32 v220, v22, v23
	v_cvt_pk_bf16_f32 v221, v24, v25
	v_cvt_pk_bf16_f32 v222, v26, v27
	v_cvt_pk_bf16_f32 v223, v28, v29
	v_cvt_pk_bf16_f32 v224, v30, v31
	v_cvt_pk_bf16_f32 v225, v32, v33
	v_cvt_pk_bf16_f32 v226, v34, v35
	v_cvt_pk_bf16_f32 v227, v36, v37
	v_cvt_pk_bf16_f32 v228, v38, v39
	v_cvt_pk_bf16_f32 v229, v40, v41
	v_cvt_pk_bf16_f32 v230, v42, v43
	v_cvt_pk_bf16_f32 v231, v44, v45
	v_cvt_pk_bf16_f32 v232, v46, v47
	v_cvt_pk_bf16_f32 v233, v48, v49
	v_cvt_pk_bf16_f32 v234, v50, v51
	v_cvt_pk_bf16_f32 v235, v52, v53
	v_cvt_pk_bf16_f32 v236, v54, v55
	v_cvt_pk_bf16_f32 v237, v56, v57
	v_cvt_pk_bf16_f32 v238, v58, v59
	v_cvt_pk_bf16_f32 v239, v60, v61
	v_cvt_pk_bf16_f32 v240, v62, v63
	v_cvt_pk_bf16_f32 v241, v64, v65
	s_waitcnt lgkmcnt(15)
	v_mfma_f32_32x32x16_bf16 v[82:97], v[74:77], v[66:69], 0
	v_mfma_f32_32x32x16_bf16 v[66:81], v[74:77], v[70:73], 0
	v_mfma_f32_32x32x16_bf16 v[82:97], v[214:217], v[114:117], v[82:97]
	v_mfma_f32_32x32x16_bf16 v[66:81], v[214:217], v[150:153], v[66:81]
	v_mfma_f32_32x32x16_bf16 v[82:97], v[218:221], v[118:121], v[82:97]
	v_mfma_f32_32x32x16_bf16 v[66:81], v[218:221], v[154:157], v[66:81]
	v_mfma_f32_32x32x16_bf16 v[82:97], v[222:225], v[122:125], v[82:97]
	v_mfma_f32_32x32x16_bf16 v[66:81], v[222:225], v[158:161], v[66:81]
	s_waitcnt lgkmcnt(14)
	v_mfma_f32_32x32x16_bf16 v[82:97], v[226:229], v[126:129], v[82:97]
	v_mfma_f32_32x32x16_bf16 v[66:81], v[226:229], v[162:165], v[66:81]
	s_waitcnt lgkmcnt(12)
	v_mfma_f32_32x32x16_bf16 v[82:97], v[230:233], v[138:141], v[82:97]
	v_mfma_f32_32x32x16_bf16 v[66:81], v[230:233], v[166:169], v[66:81]
	s_waitcnt lgkmcnt(10)
	v_mfma_f32_32x32x16_bf16 v[82:97], v[234:237], v[142:145], v[82:97]
	v_mfma_f32_32x32x16_bf16 v[66:81], v[234:237], v[170:173], v[66:81]
	s_waitcnt lgkmcnt(8)
	v_mfma_f32_32x32x16_bf16 v[82:97], v[238:241], v[146:149], v[82:97]
	v_mfma_f32_32x32x16_bf16 v[66:81], v[238:241], v[174:177], v[66:81]
	s_waitcnt lgkmcnt(6)
	v_mfma_f32_32x32x16_bf16 v[82:97], v[110:113], v[178:181], v[82:97]
	v_mfma_f32_32x32x16_bf16 v[66:81], v[110:113], v[198:201], v[66:81]
	s_waitcnt lgkmcnt(4)
	v_mfma_f32_32x32x16_bf16 v[82:97], v[106:109], v[182:185], v[82:97]
	v_mfma_f32_32x32x16_bf16 v[66:81], v[106:109], v[202:205], v[66:81]
	s_waitcnt lgkmcnt(2)
	v_mfma_f32_32x32x16_bf16 v[82:97], v[102:105], v[186:189], v[82:97]
	v_mfma_f32_32x32x16_bf16 v[66:81], v[102:105], v[206:209], v[66:81]
	s_waitcnt lgkmcnt(0)
	v_mfma_f32_32x32x16_bf16 v[82:97], v[98:101], v[190:193], v[82:97]
	v_mfma_f32_32x32x16_bf16 v[66:81], v[98:101], v[210:213], v[66:81]
	v_lshl_add_u32 v132, s7, 6, v1
	v_lshlrev_b64 v[114:115], 11, v[132:133]
	v_lshl_add_u64 v[114:115], v[134:135], 0, v[114:115]
	v_cvt_pk_bf16_f32 v82, v82, v83
	v_cvt_pk_bf16_f32 v83, v84, v85
	s_nop 7
	global_store_dwordx2 v[114:115], v[82:83], off
	v_cvt_pk_bf16_f32 v82, v86, v87
	v_cvt_pk_bf16_f32 v83, v88, v89
	global_store_dwordx2 v[114:115], v[82:83], off offset:16
	v_cvt_pk_bf16_f32 v82, v90, v91
	v_cvt_pk_bf16_f32 v83, v92, v93
	global_store_dwordx2 v[114:115], v[82:83], off offset:32
	v_cvt_pk_bf16_f32 v82, v94, v95
	v_cvt_pk_bf16_f32 v83, v96, v97
	v_or_b32_e32 v132, 32, v132
	global_store_dwordx2 v[114:115], v[82:83], off offset:48
	v_lshlrev_b64 v[82:83], 11, v[132:133]
	v_lshl_add_u64 v[82:83], v[134:135], 0, v[82:83]
	v_cvt_pk_bf16_f32 v66, v66, v67
	v_cvt_pk_bf16_f32 v67, v68, v69
	global_store_dwordx2 v[82:83], v[66:67], off
	v_cvt_pk_bf16_f32 v66, v70, v71
	v_cvt_pk_bf16_f32 v67, v72, v73
	global_store_dwordx2 v[82:83], v[66:67], off offset:16
	v_cvt_pk_bf16_f32 v66, v74, v75
	v_cvt_pk_bf16_f32 v67, v76, v77
	global_store_dwordx2 v[82:83], v[66:67], off offset:32
	v_cvt_pk_bf16_f32 v66, v78, v79
	v_cvt_pk_bf16_f32 v67, v80, v81
	global_store_dwordx2 v[82:83], v[66:67], off offset:48
	s_branch .LBB0_557
